# layer-0 Hyena context units reassigned to workgroups that carry six (not seven) attention units
# baseline (speedup 1.0000x reference)
.LBB0_310:
	s_lshl_b32 s4, s2, 3
	v_writelane_b32 v254, s4, 7
	s_lshl_b32 s4, s3, 3
	v_writelane_b32 v254, s4, 8
	s_lshl_b32 s4, s2, 9
	s_lshl_b32 s62, s3, 9
	s_cmp_eq_u32 s2, 0
	v_writelane_b32 v254, s4, 9
	s_cselect_b64 s[4:5], -1, 0
	v_writelane_b32 v254, s4, 10
	s_lshl_b32 s8, s2, 5
	s_and_b32 s14, s87, 31
	v_writelane_b32 v254, s5, 11
	s_mul_i32 s4, s2, 0x6b
	s_add_i32 s7, s4, 0xffffd954
	s_ashr_i32 s11, s87, 5
	s_lshl_b32 s4, s2, 4
	s_lshl_b32 s66, s3, 4
	s_cmpk_lt_i32 s2, 0x100
	v_writelane_b32 v254, s4, 12
	s_cselect_b64 s[4:5], -1, 0
	v_writelane_b32 v254, s4, 13
	s_movk_i32 s64, 0x80
	s_movk_i32 s65, 0xff00
	v_writelane_b32 v254, s5, 14
	s_lshr_b32 s4, s2, 3
	s_mul_i32 s4, s4, 5
	s_and_b32 s5, s2, 7
	s_add_i32 s4, s4, s5
	s_add_i32 s4, s4, -3
	s_cmp_lt_u32 s5, 3
	s_cselect_b32 s4, 0x7fff, s4
	s_cmpk_lt_i32 s4, 0x80
	v_writelane_b32 v254, s4, 15
	s_cselect_b64 s[4:5], -1, 0
	s_and_b32 s9, s87, 3
	v_writelane_b32 v254, s4, 16
	s_cmpk_lt_i32 s2, 0x200
	s_movk_i32 s56, 0x1000
	v_writelane_b32 v254, s5, 17
	s_cselect_b64 s[4:5], -1, 0
	v_writelane_b32 v254, s4, 18
	s_lshl_b32 s74, s3, 5
	s_movk_i32 s77, 0x4400
	v_writelane_b32 v254, s5, 19
	s_lshl_b32 s4, s2, 2
	s_and_b32 s4, s4, 0xffffff00
	v_writelane_b32 v254, s4, 20
	s_lshl_b32 s4, s2, 6
	s_and_b32 s6, s4, 0xfc0
	s_cmp_gt_i32 s3, 0
	v_writelane_b32 v254, s4, 21
	s_cselect_b64 s[4:5], -1, 0
	v_writelane_b32 v254, s4, 22
	s_ashr_i32 s12, s87, 2
	s_mov_b32 s10, s12
	v_writelane_b32 v254, s5, 23
	s_ashr_i32 s4, s87, 3
	v_writelane_b32 v254, s4, 24
	s_and_b32 s5, s87, 7
	s_lshl_b32 s4, s5, 7
	v_writelane_b32 v254, s5, 25
	s_lshl_b32 s5, s5, 18
	v_writelane_b32 v254, s5, 26
	s_ashr_i32 s13, s12, 31
	v_writelane_b32 v254, s10, 27
	s_lshl_b64 s[12:13], s[12:13], 18
	s_lshl_b32 s5, s9, 8
	v_writelane_b32 v254, s11, 28
	v_writelane_b32 v254, s12, 29
	s_mov_b32 s38, 0x78787879
	s_movk_i32 s39, 0xef00
	v_writelane_b32 v254, s13, 30
	v_writelane_b32 v254, s9, 31
	s_lshl_b32 s9, s9, 18
	s_cmpk_lt_i32 s2, 0x84
	v_writelane_b32 v254, s9, 32
	s_cselect_b32 s9, 32, 0x6b
	v_writelane_b32 v254, s9, 33
	v_writelane_b32 v254, s8, 34
	s_cselect_b32 s7, s8, s7
	v_writelane_b32 v254, s7, 35
	s_add_i32 s7, s3, -1
	s_cmp_gt_u32 s7, 6
	s_cselect_b64 s[8:9], -1, 0
	s_abs_i32 s12, s3
	v_cvt_f32_u32_e32 v1, s12
	v_writelane_b32 v254, s8, 36
	s_sub_i32 s7, 0, s12
	s_and_b32 s76, s3, 0x7ffffff8
	v_rcp_iflag_f32_e32 v1, v1
	v_writelane_b32 v254, s9, 37
	s_ashr_i32 s13, s3, 31
	s_mov_b32 s59, 0x800000
	v_mul_f32_e32 v1, 0x4f7ffffe, v1
	v_cvt_u32_f32_e32 v1, v1
	v_mov_b32_e32 v205, 1
	v_mov_b32_e32 v221, 0x1400
	v_mov_b32_e32 v204, 0x20200
	v_readfirstlane_b32 s8, v1
	s_mul_i32 s7, s7, s8
	s_mul_hi_u32 s7, s8, s7
	s_add_i32 s7, s8, s7
	v_writelane_b32 v254, s7, 38
	s_mul_hi_u32 s7, s7, 0x6d3
	s_mul_i32 s8, s7, s12
	s_sub_i32 s8, 0x6d3, s8
	s_add_i32 s9, s7, 1
	s_sub_i32 s10, s8, s12
	s_cmp_ge_u32 s8, s12
	s_cselect_b32 s7, s9, s7
	s_cselect_b32 s8, s10, s8
	s_add_i32 s9, s7, 1
	s_cmp_ge_u32 s8, s12
	s_cselect_b32 s7, s9, s7
	s_xor_b32 s7, s7, s13
	s_sub_i32 s7, s7, s13
	s_mul_i32 s8, s7, s3
	s_sub_i32 s8, 0x6d3, s8
	s_mul_i32 s9, s7, s87
	s_min_i32 s10, s87, s8
	v_writelane_b32 v254, s12, 39
	s_add_i32 s9, s9, s10
	v_writelane_b32 v254, s13, 40
	s_cmp_lt_i32 s87, s8
	v_writelane_b32 v254, s9, 41
	s_cselect_b64 s[8:9], -1, 0
	s_cmp_lg_u64 s[8:9], 0
	s_addc_u32 s7, s7, 0
	v_writelane_b32 v254, s7, 42
	s_lshl_b32 s7, s3, 1
	v_writelane_b32 v254, s7, 43
	s_add_i32 s7, s11, 17
	v_writelane_b32 v254, s7, 44
	s_lshl_b32 s7, s7, 4
	v_writelane_b32 v254, s7, 45
	s_lshl_b32 s7, s14, 4
	v_writelane_b32 v254, s14, 46
	s_add_i32 s8, s7, 0xd250
	v_writelane_b32 v254, s8, 47
	s_add_i32 s8, s11, 9
	v_writelane_b32 v254, s8, 48
	s_lshl_b32 s8, s8, 4
	v_writelane_b32 v254, s8, 49
	v_writelane_b32 v254, s11, 50
	s_add_i32 s8, s11, 1
	v_writelane_b32 v254, s8, 51
	s_or_b32 s8, s7, 0xfffffe00
	v_writelane_b32 v254, s8, 52
	s_lshl_b32 s8, s3, 6
	v_writelane_b32 v254, s8, 53
	s_add_i32 s7, s7, 0xa050
	v_writelane_b32 v254, s7, 54
	s_add_i32 s7, 0, 0x12000
	v_writelane_b32 v254, s7, 55
	s_add_i32 s7, 0, 0x27020
	v_writelane_b32 v254, s7, 56
	s_add_i32 s7, 0, 0x27024
	v_writelane_b32 v254, s7, 57
	s_add_i32 s7, 0, 0x25000
	v_writelane_b32 v254, s7, 58
	s_lshl_b32 s6, s6, 1
	v_writelane_b32 v254, s6, 59
	s_lshl_b32 s5, s5, 2
	v_writelane_b32 v254, s5, 60
	s_add_i32 s5, 0, 0x25400
	v_writelane_b32 v254, s5, 61
	s_add_i32 s5, 0, 0x10200
	v_writelane_b32 v254, s5, 62
	s_add_i32 s5, 0, 0x20100
	v_writelane_b32 v254, s5, 63
	s_add_i32 s5, 0, 0x20010
	v_writelane_b32 v255, s5, 0
	s_add_i32 s5, 0, 0x20110
	v_writelane_b32 v255, s5, 1
	s_add_i32 s5, 0, 0x20020
	v_writelane_b32 v255, s5, 2
	s_add_i32 s5, 0, 0x20120
	v_writelane_b32 v255, s5, 3
	s_add_i32 s5, 0, 0x20030
	v_writelane_b32 v255, s5, 4
	s_add_i32 s5, 0, 0x20130
	v_writelane_b32 v255, s5, 5
	s_add_i32 s5, 0, 0x20040
	v_writelane_b32 v255, s5, 6
	s_add_i32 s5, 0, 0x20140
	v_writelane_b32 v255, s5, 7
	s_add_i32 s5, 0, 0x20050
	v_writelane_b32 v255, s5, 8
	s_add_i32 s5, 0, 0x20150
	v_writelane_b32 v255, s5, 9
	s_add_i32 s5, 0, 0x20060
	v_writelane_b32 v255, s5, 10
	s_add_i32 s5, 0, 0x20160
	v_writelane_b32 v255, s5, 11
	s_add_i32 s5, 0, 0x20070
	v_writelane_b32 v255, s5, 12
	s_add_i32 s5, 0, 0x20170
	v_writelane_b32 v255, s5, 13
	s_add_i32 s5, 0, 0x20180
	v_writelane_b32 v255, s5, 14
	s_add_i32 s5, 0, 0x20084
	v_writelane_b32 v255, s5, 15
	s_add_i32 s5, 0, 0x20024
	v_writelane_b32 v255, s5, 16
	s_add_i32 s5, 0, 0x2002c
	v_writelane_b32 v255, s5, 17
	s_add_i32 s5, 0, 0x20034
	v_writelane_b32 v255, s5, 18
	s_add_i32 s5, 0, 0x2003c
	v_writelane_b32 v255, s5, 19
	s_add_i32 s5, 0, 0x20044
	v_writelane_b32 v255, s5, 20
	s_add_i32 s5, 0, 0x2004c
	v_writelane_b32 v255, s5, 21
	s_add_i32 s5, 0, 0x20054
	v_writelane_b32 v255, s5, 22
	s_add_i32 s5, 0, 0x2005c
	v_writelane_b32 v255, s5, 23
	s_add_i32 s5, 0, 0x20064
	v_writelane_b32 v255, s5, 24
	s_add_i32 s5, 0, 0x2006c
	v_writelane_b32 v255, s5, 25
	s_add_i32 s5, 0, 0x20074
	v_writelane_b32 v255, s5, 26
	s_add_i32 s5, 0, 0x2007c
	v_writelane_b32 v255, s5, 27
	s_add_i32 s5, 0, 0x20800
	v_writelane_b32 v255, s5, 28
	s_lshl_b32 s4, s4, 2
	v_writelane_b32 v255, s4, 29
	s_ashr_i32 s63, s62, 31
	s_ashr_i32 s67, s66, 31
	v_writelane_b32 v255, s5, 30
	v_cmp_eq_u32_e64 s[4:5], 0, v0
	s_mov_b32 s6, s74
	s_add_i32 s84, 0, 0x20004
	v_writelane_b32 v255, s4, 31
	s_add_i32 s69, 0, 0x2000c
	s_add_i32 s68, 0, 0x20014
	v_writelane_b32 v255, s5, 32
	s_lshl_b64 s[4:5], s[62:63], 2
	v_writelane_b32 v255, s4, 33
	s_add_i32 s49, 0, 0x2001c
	v_mov_b32_e32 v1, 0
	v_writelane_b32 v255, s5, 34
	s_lshl_b64 s[4:5], s[66:67], 12
	v_writelane_b32 v255, s4, 35
	v_mov_b32_e32 v220, 0xff800000
	s_movk_i32 s47, 0x3ff
	v_writelane_b32 v255, s5, 36
	v_writelane_b32 v255, s6, 37
	s_mov_b32 s83, 0x34400000
	s_mov_b32 s80, 0x36500000
	v_writelane_b32 v255, s7, 38
	s_mov_b32 s6, s62
	v_writelane_b32 v255, s6, 39
	s_movk_i32 s81, 0x7fff
	s_mov_b32 s57, 0x41000000
	v_writelane_b32 v255, s7, 40
	s_mov_b32 s6, s66
	v_writelane_b32 v255, s6, 41
	s_movk_i32 s33, 0xfefe
	s_mov_b32 s85, 0x900000
	v_writelane_b32 v255, s7, 42
	v_writelane_b32 v255, s76, 43
	v_writelane_b32 v255, s84, 44
	s_mov_b32 s72, 0xc0e00000
	s_mov_b32 s73, 0
	s_mov_b32 s71, 0
	s_mov_b64 s[4:5], -1
	s_mov_b64 s[78:79], 0x80
	s_mov_b32 s82, 0x3e38aa3b
	s_mov_b32 s88, 0xc01d265f
	s_mov_b32 s50, s69
	s_mov_b32 s86, s68
	s_mov_b32 s60, s49
	v_writelane_b32 v255, s87, 45
	s_branch .LBB0_314
